# scanA Neumann T-update: hoist serialized acc-init LDS reads, interleave 4 MFMA chains
# speedup vs baseline: 1.5362x; 1.0107x over previous
.LBB0_598:
	s_waitcnt lgkmcnt(0)
	v_cndmask_b32_e64 v8, 0, 1, s[26:27]
	v_add_u32_e32 v25, s76, v28
	v_cmp_ne_u32_e64 s[46:47], 1, v8
	s_andn2_b64 vcc, exec, s[26:27]
	s_mov_b64 s[72:73], -1
	s_waitcnt lgkmcnt(0)
	s_barrier
	s_cbranch_vccnz .LBB0_604
	s_and_b64 vcc, exec, s[44:45]
	s_cbranch_vccnz .LBB0_601
	s_add_i32 s35, 0, 0x16800
	v_add3_u32 v8, s35, v24, v75
	ds_read_b128 v[16:19], v8
	ds_read_b128 v[8:11], v8 offset:64
	v_add_u32_e32 v156, s35, v79
	ds_read_b64 v[158:159], v156
	ds_read_b64 v[160:161], v156 offset:32
	ds_read_b64 v[162:163], v156 offset:64
	ds_read_b64 v[164:165], v156 offset:96
	ds_read_b64_tr_b16 v[112:113], v25
	ds_read_b64_tr_b16 v[114:115], v25 offset:576
	ds_read_b64_tr_b16 v[80:81], v25 offset:4608
	ds_read_b64_tr_b16 v[82:83], v25 offset:5184
	ds_read_b64_tr_b16 v[42:43], v25 offset:32
	ds_read_b64_tr_b16 v[44:45], v25 offset:608
	ds_read_b64_tr_b16 v[38:39], v25 offset:4640
	ds_read_b64_tr_b16 v[40:41], v25 offset:5216
	ds_read_b64_tr_b16 v[34:35], v25 offset:64
	ds_read_b64_tr_b16 v[36:37], v25 offset:640
	ds_read_b64_tr_b16 v[30:31], v25 offset:4672
	ds_read_b64_tr_b16 v[32:33], v25 offset:5248
	ds_read_b64_tr_b16 v[20:21], v25 offset:96
	ds_read_b64_tr_b16 v[22:23], v25 offset:672
	ds_read_b64_tr_b16 v[12:13], v25 offset:4704
	ds_read_b64_tr_b16 v[14:15], v25 offset:5280
	s_waitcnt lgkmcnt(0)
	v_add_u32_e32 v157, s75, v79
	v_lshlrev_b32_e32 v166, 16, v158
	v_and_b32_e32 v167, 0xffff0000, v158
	v_lshlrev_b32_e32 v168, 16, v159
	v_and_b32_e32 v169, 0xffff0000, v159
	v_lshlrev_b32_e32 v170, 16, v160
	v_and_b32_e32 v171, 0xffff0000, v160
	v_lshlrev_b32_e32 v172, 16, v161
	v_and_b32_e32 v173, 0xffff0000, v161
	v_lshlrev_b32_e32 v174, 16, v162
	v_and_b32_e32 v175, 0xffff0000, v162
	v_lshlrev_b32_e32 v176, 16, v163
	v_and_b32_e32 v177, 0xffff0000, v163
	v_lshlrev_b32_e32 v178, 16, v164
	v_and_b32_e32 v179, 0xffff0000, v164
	v_lshlrev_b32_e32 v180, 16, v165
	v_and_b32_e32 v181, 0xffff0000, v165
	v_mfma_f32_16x16x32_bf16 v[112:115], v[112:115], v[16:19], v[166:169]
	v_mfma_f32_16x16x32_bf16 v[42:45], v[42:45], v[16:19], v[170:173]
	v_mfma_f32_16x16x32_bf16 v[34:37], v[34:37], v[16:19], v[174:177]
	v_mfma_f32_16x16x32_bf16 v[20:23], v[20:23], v[16:19], v[178:181]
	v_mfma_f32_16x16x32_bf16 v[80:83], v[80:83], v[8:11], v[112:115]
	v_mfma_f32_16x16x32_bf16 v[38:41], v[38:41], v[8:11], v[42:45]
	v_mfma_f32_16x16x32_bf16 v[30:33], v[30:33], v[8:11], v[34:37]
	v_mfma_f32_16x16x32_bf16 v[12:15], v[12:15], v[8:11], v[20:23]
	s_nop 7
	v_cvt_pk_bf16_f32 v182, v80, v81
	v_cvt_pk_bf16_f32 v183, v82, v83
	v_cvt_pk_bf16_f32 v184, v38, v39
	v_cvt_pk_bf16_f32 v185, v40, v41
	v_cvt_pk_bf16_f32 v186, v30, v31
	v_cvt_pk_bf16_f32 v187, v32, v33
	v_cvt_pk_bf16_f32 v188, v12, v13
	v_cvt_pk_bf16_f32 v189, v14, v15
	ds_write_b64 v157, v[182:183]
	ds_write_b64 v157, v[184:185] offset:32
	ds_write_b64 v157, v[186:187] offset:64
	ds_write_b64 v157, v[188:189] offset:96
	s_mov_b64 s[72:73], 0

.LBB0_604:
	s_andn2_b64 vcc, exec, s[72:73]
	s_cbranch_vccnz .LBB0_609
	s_and_b64 vcc, exec, s[44:45]
	s_mov_b64 s[72:73], -1
	s_cbranch_vccnz .LBB0_607
	s_add_i32 s35, 0, 0x16800
	s_nop 1
	v_add3_u32 v8, s35, v24, v75
	ds_read_b128 v[8:11], v8
	v_add_u32_e32 v156, s35, v79
	ds_read_b64 v[158:159], v156
	ds_read_b64 v[160:161], v156 offset:32
	ds_read_b64_tr_b16 v[16:17], v25
	ds_read_b64_tr_b16 v[18:19], v25 offset:576
	ds_read_b64_tr_b16 v[12:13], v25 offset:32
	ds_read_b64_tr_b16 v[14:15], v25 offset:608
	s_waitcnt lgkmcnt(0)
	v_add_u32_e32 v157, s75, v79
	v_lshlrev_b32_e32 v166, 16, v158
	v_and_b32_e32 v167, 0xffff0000, v158
	v_lshlrev_b32_e32 v168, 16, v159
	v_and_b32_e32 v169, 0xffff0000, v159
	v_lshlrev_b32_e32 v170, 16, v160
	v_and_b32_e32 v171, 0xffff0000, v160
	v_lshlrev_b32_e32 v172, 16, v161
	v_and_b32_e32 v173, 0xffff0000, v161
	s_nop 1
	v_mfma_f32_16x16x32_bf16 v[16:19], v[16:19], v[8:11], v[166:169]
	v_mfma_f32_16x16x32_bf16 v[12:15], v[12:15], v[8:11], v[170:173]
	s_nop 7
	v_cvt_pk_bf16_f32 v182, v16, v17
	v_cvt_pk_bf16_f32 v183, v18, v19
	v_cvt_pk_bf16_f32 v184, v12, v13
	v_cvt_pk_bf16_f32 v185, v14, v15
	ds_write_b64 v157, v[182:183]
	ds_write_b64 v157, v[184:185] offset:32
	s_mov_b64 s[72:73], 0

.LBB0_609:
	s_waitcnt lgkmcnt(0)
	s_add_i32 s35, 0, 0x12000
	v_add_u32_e32 v34, s35, v28
	s_and_b64 vcc, exec, s[46:47]
	s_mov_b64 s[72:73], -1
	s_waitcnt lgkmcnt(0)
	s_barrier
	s_cbranch_vccnz .LBB0_615
	s_and_b64 vcc, exec, s[44:45]
	s_cbranch_vccnz .LBB0_612
	s_add_i32 s72, 0, 0x16800
	v_add3_u32 v8, s75, v24, v75
	ds_read_b128 v[16:19], v8
	ds_read_b128 v[8:11], v8 offset:64
	v_add_u32_e32 v156, s75, v79
	ds_read_b64 v[158:159], v156
	ds_read_b64 v[160:161], v156 offset:32
	ds_read_b64 v[162:163], v156 offset:64
	ds_read_b64 v[164:165], v156 offset:96
	ds_read_b64_tr_b16 v[112:113], v34
	ds_read_b64_tr_b16 v[114:115], v34 offset:576
	ds_read_b64_tr_b16 v[80:81], v34 offset:4608
	ds_read_b64_tr_b16 v[82:83], v34 offset:5184
	ds_read_b64_tr_b16 v[44:45], v34 offset:32
	ds_read_b64_tr_b16 v[46:47], v34 offset:608
	ds_read_b64_tr_b16 v[40:41], v34 offset:4640
	ds_read_b64_tr_b16 v[42:43], v34 offset:5216
	ds_read_b64_tr_b16 v[36:37], v34 offset:64
	ds_read_b64_tr_b16 v[38:39], v34 offset:640
	ds_read_b64_tr_b16 v[30:31], v34 offset:4672
	ds_read_b64_tr_b16 v[32:33], v34 offset:5248
	ds_read_b64_tr_b16 v[20:21], v34 offset:96
	ds_read_b64_tr_b16 v[22:23], v34 offset:672
	ds_read_b64_tr_b16 v[12:13], v34 offset:4704
	ds_read_b64_tr_b16 v[14:15], v34 offset:5280
	s_waitcnt lgkmcnt(0)
	v_add_u32_e32 v157, s72, v79
	v_lshlrev_b32_e32 v166, 16, v158
	v_and_b32_e32 v167, 0xffff0000, v158
	v_lshlrev_b32_e32 v168, 16, v159
	v_and_b32_e32 v169, 0xffff0000, v159
	v_lshlrev_b32_e32 v170, 16, v160
	v_and_b32_e32 v171, 0xffff0000, v160
	v_lshlrev_b32_e32 v172, 16, v161
	v_and_b32_e32 v173, 0xffff0000, v161
	v_lshlrev_b32_e32 v174, 16, v162
	v_and_b32_e32 v175, 0xffff0000, v162
	v_lshlrev_b32_e32 v176, 16, v163
	v_and_b32_e32 v177, 0xffff0000, v163
	v_lshlrev_b32_e32 v178, 16, v164
	v_and_b32_e32 v179, 0xffff0000, v164
	v_lshlrev_b32_e32 v180, 16, v165
	v_and_b32_e32 v181, 0xffff0000, v165
	v_mfma_f32_16x16x32_bf16 v[112:115], v[112:115], v[16:19], v[166:169]
	v_mfma_f32_16x16x32_bf16 v[44:47], v[44:47], v[16:19], v[170:173]
	v_mfma_f32_16x16x32_bf16 v[36:39], v[36:39], v[16:19], v[174:177]
	v_mfma_f32_16x16x32_bf16 v[20:23], v[20:23], v[16:19], v[178:181]
	v_mfma_f32_16x16x32_bf16 v[80:83], v[80:83], v[8:11], v[112:115]
	v_mfma_f32_16x16x32_bf16 v[40:43], v[40:43], v[8:11], v[44:47]
	v_mfma_f32_16x16x32_bf16 v[30:33], v[30:33], v[8:11], v[36:39]
	v_mfma_f32_16x16x32_bf16 v[12:15], v[12:15], v[8:11], v[20:23]
	s_nop 7
	v_cvt_pk_bf16_f32 v182, v80, v81
	v_cvt_pk_bf16_f32 v183, v82, v83
	v_cvt_pk_bf16_f32 v184, v40, v41
	v_cvt_pk_bf16_f32 v185, v42, v43
	v_cvt_pk_bf16_f32 v186, v30, v31
	v_cvt_pk_bf16_f32 v187, v32, v33
	v_cvt_pk_bf16_f32 v188, v12, v13
	v_cvt_pk_bf16_f32 v189, v14, v15
	ds_write_b64 v157, v[182:183]
	ds_write_b64 v157, v[184:185] offset:32
	ds_write_b64 v157, v[186:187] offset:64
	ds_write_b64 v157, v[188:189] offset:96
	s_mov_b64 s[72:73], 0

.LBB0_615:
	s_andn2_b64 vcc, exec, s[72:73]
	s_cbranch_vccnz .LBB0_620
	s_and_b64 vcc, exec, s[44:45]
	s_mov_b64 s[72:73], -1
	s_cbranch_vccnz .LBB0_618
	s_add_i32 s52, 0, 0x16800
	s_nop 1
	v_add3_u32 v8, s75, v24, v75
	ds_read_b128 v[8:11], v8
	v_add_u32_e32 v156, s75, v79
	ds_read_b64 v[158:159], v156
	ds_read_b64 v[160:161], v156 offset:32
	ds_read_b64_tr_b16 v[16:17], v34
	ds_read_b64_tr_b16 v[18:19], v34 offset:576
	ds_read_b64_tr_b16 v[12:13], v34 offset:32
	ds_read_b64_tr_b16 v[14:15], v34 offset:608
	s_waitcnt lgkmcnt(0)
	v_add_u32_e32 v157, s52, v79
	v_lshlrev_b32_e32 v166, 16, v158
	v_and_b32_e32 v167, 0xffff0000, v158
	v_lshlrev_b32_e32 v168, 16, v159
	v_and_b32_e32 v169, 0xffff0000, v159
	v_lshlrev_b32_e32 v170, 16, v160
	v_and_b32_e32 v171, 0xffff0000, v160
	v_lshlrev_b32_e32 v172, 16, v161
	v_and_b32_e32 v173, 0xffff0000, v161
	s_nop 1
	v_mfma_f32_16x16x32_bf16 v[16:19], v[16:19], v[8:11], v[166:169]
	v_mfma_f32_16x16x32_bf16 v[12:15], v[12:15], v[8:11], v[170:173]
	s_nop 7
	v_cvt_pk_bf16_f32 v182, v16, v17
	v_cvt_pk_bf16_f32 v183, v18, v19
	v_cvt_pk_bf16_f32 v184, v12, v13
	v_cvt_pk_bf16_f32 v185, v14, v15
	ds_write_b64 v157, v[182:183]
	ds_write_b64 v157, v[184:185] offset:32
	s_mov_b64 s[72:73], 0

.LBB0_620:
	s_waitcnt lgkmcnt(0)
	s_and_b64 vcc, exec, s[46:47]
	s_mov_b64 s[72:73], -1
	s_waitcnt lgkmcnt(0)
	s_barrier
	s_cbranch_vccnz .LBB0_626
	s_and_b64 vcc, exec, s[44:45]
	s_cbranch_vccnz .LBB0_623
	s_add_i32 s72, 0, 0x16800
	v_add3_u32 v8, s72, v24, v75
	ds_read_b128 v[16:19], v8
	ds_read_b128 v[8:11], v8 offset:64
	v_add_u32_e32 v156, s72, v79
	ds_read_b64 v[158:159], v156
	ds_read_b64 v[160:161], v156 offset:32
	ds_read_b64 v[162:163], v156 offset:64
	ds_read_b64 v[164:165], v156 offset:96
	ds_read_b64_tr_b16 v[112:113], v25
	ds_read_b64_tr_b16 v[114:115], v25 offset:576
	ds_read_b64_tr_b16 v[80:81], v25 offset:4608
	ds_read_b64_tr_b16 v[82:83], v25 offset:5184
	ds_read_b64_tr_b16 v[44:45], v25 offset:32
	ds_read_b64_tr_b16 v[46:47], v25 offset:608
	ds_read_b64_tr_b16 v[40:41], v25 offset:4640
	ds_read_b64_tr_b16 v[42:43], v25 offset:5216
	ds_read_b64_tr_b16 v[36:37], v25 offset:64
	ds_read_b64_tr_b16 v[38:39], v25 offset:640
	ds_read_b64_tr_b16 v[30:31], v25 offset:4672
	ds_read_b64_tr_b16 v[32:33], v25 offset:5248
	ds_read_b64_tr_b16 v[20:21], v25 offset:96
	ds_read_b64_tr_b16 v[22:23], v25 offset:672
	ds_read_b64_tr_b16 v[12:13], v25 offset:4704
	ds_read_b64_tr_b16 v[14:15], v25 offset:5280
	s_waitcnt lgkmcnt(0)
	v_add_u32_e32 v157, s75, v79
	v_lshlrev_b32_e32 v166, 16, v158
	v_and_b32_e32 v167, 0xffff0000, v158
	v_lshlrev_b32_e32 v168, 16, v159
	v_and_b32_e32 v169, 0xffff0000, v159
	v_lshlrev_b32_e32 v170, 16, v160
	v_and_b32_e32 v171, 0xffff0000, v160
	v_lshlrev_b32_e32 v172, 16, v161
	v_and_b32_e32 v173, 0xffff0000, v161
	v_lshlrev_b32_e32 v174, 16, v162
	v_and_b32_e32 v175, 0xffff0000, v162
	v_lshlrev_b32_e32 v176, 16, v163
	v_and_b32_e32 v177, 0xffff0000, v163
	v_lshlrev_b32_e32 v178, 16, v164
	v_and_b32_e32 v179, 0xffff0000, v164
	v_lshlrev_b32_e32 v180, 16, v165
	v_and_b32_e32 v181, 0xffff0000, v165
	v_mfma_f32_16x16x32_bf16 v[112:115], v[112:115], v[16:19], v[166:169]
	v_mfma_f32_16x16x32_bf16 v[44:47], v[44:47], v[16:19], v[170:173]
	v_mfma_f32_16x16x32_bf16 v[36:39], v[36:39], v[16:19], v[174:177]
	v_mfma_f32_16x16x32_bf16 v[20:23], v[20:23], v[16:19], v[178:181]
	v_mfma_f32_16x16x32_bf16 v[80:83], v[80:83], v[8:11], v[112:115]
	v_mfma_f32_16x16x32_bf16 v[40:43], v[40:43], v[8:11], v[44:47]
	v_mfma_f32_16x16x32_bf16 v[30:33], v[30:33], v[8:11], v[36:39]
	v_mfma_f32_16x16x32_bf16 v[12:15], v[12:15], v[8:11], v[20:23]
	s_nop 7
	v_cvt_pk_bf16_f32 v182, v80, v81
	v_cvt_pk_bf16_f32 v183, v82, v83
	v_cvt_pk_bf16_f32 v184, v40, v41
	v_cvt_pk_bf16_f32 v185, v42, v43
	v_cvt_pk_bf16_f32 v186, v30, v31
	v_cvt_pk_bf16_f32 v187, v32, v33
	v_cvt_pk_bf16_f32 v188, v12, v13
	v_cvt_pk_bf16_f32 v189, v14, v15
	ds_write_b64 v157, v[182:183]
	ds_write_b64 v157, v[184:185] offset:32
	ds_write_b64 v157, v[186:187] offset:64
	ds_write_b64 v157, v[188:189] offset:96
	s_mov_b64 s[72:73], 0

.LBB0_626:
	s_andn2_b64 vcc, exec, s[72:73]
	s_cbranch_vccnz .LBB0_631
	s_and_b64 vcc, exec, s[44:45]
	s_mov_b64 s[72:73], -1
	s_cbranch_vccnz .LBB0_629
	s_add_i32 s52, 0, 0x16800
	s_nop 1
	v_add3_u32 v8, s52, v24, v75
	ds_read_b128 v[8:11], v8
	v_add_u32_e32 v156, s52, v79
	ds_read_b64 v[158:159], v156
	ds_read_b64 v[160:161], v156 offset:32
	ds_read_b64_tr_b16 v[16:17], v25
	ds_read_b64_tr_b16 v[18:19], v25 offset:576
	ds_read_b64_tr_b16 v[12:13], v25 offset:32
	ds_read_b64_tr_b16 v[14:15], v25 offset:608
	s_waitcnt lgkmcnt(0)
	v_add_u32_e32 v157, s75, v79
	v_lshlrev_b32_e32 v166, 16, v158
	v_and_b32_e32 v167, 0xffff0000, v158
	v_lshlrev_b32_e32 v168, 16, v159
	v_and_b32_e32 v169, 0xffff0000, v159
	v_lshlrev_b32_e32 v170, 16, v160
	v_and_b32_e32 v171, 0xffff0000, v160
	v_lshlrev_b32_e32 v172, 16, v161
	v_and_b32_e32 v173, 0xffff0000, v161
	s_nop 1
	v_mfma_f32_16x16x32_bf16 v[16:19], v[16:19], v[8:11], v[166:169]
	v_mfma_f32_16x16x32_bf16 v[12:15], v[12:15], v[8:11], v[170:173]
	s_nop 7
	v_cvt_pk_bf16_f32 v182, v16, v17
	v_cvt_pk_bf16_f32 v183, v18, v19
	v_cvt_pk_bf16_f32 v184, v12, v13
	v_cvt_pk_bf16_f32 v185, v14, v15
	ds_write_b64 v157, v[182:183]
	ds_write_b64 v157, v[184:185] offset:32
	s_mov_b64 s[72:73], 0

.LBB0_631:
	s_waitcnt lgkmcnt(0)
	s_and_b64 vcc, exec, s[46:47]
	s_mov_b64 s[72:73], -1
	s_waitcnt lgkmcnt(0)
	s_barrier
	s_cbranch_vccnz .LBB0_637
	s_and_b64 vcc, exec, s[44:45]
	s_cbranch_vccnz .LBB0_634
	s_add_i32 s72, 0, 0x16800
	v_add3_u32 v8, s75, v24, v75
	ds_read_b128 v[16:19], v8
	ds_read_b128 v[8:11], v8 offset:64
	v_add_u32_e32 v156, s75, v79
	ds_read_b64 v[158:159], v156
	ds_read_b64 v[160:161], v156 offset:32
	ds_read_b64 v[162:163], v156 offset:64
	ds_read_b64 v[164:165], v156 offset:96
	ds_read_b64_tr_b16 v[112:113], v34
	ds_read_b64_tr_b16 v[114:115], v34 offset:576
	ds_read_b64_tr_b16 v[80:81], v34 offset:4608
	ds_read_b64_tr_b16 v[82:83], v34 offset:5184
	ds_read_b64_tr_b16 v[44:45], v34 offset:32
	ds_read_b64_tr_b16 v[46:47], v34 offset:608
	ds_read_b64_tr_b16 v[40:41], v34 offset:4640
	ds_read_b64_tr_b16 v[42:43], v34 offset:5216
	ds_read_b64_tr_b16 v[36:37], v34 offset:64
	ds_read_b64_tr_b16 v[38:39], v34 offset:640
	ds_read_b64_tr_b16 v[30:31], v34 offset:4672
	ds_read_b64_tr_b16 v[32:33], v34 offset:5248
	ds_read_b64_tr_b16 v[20:21], v34 offset:96
	ds_read_b64_tr_b16 v[22:23], v34 offset:672
	ds_read_b64_tr_b16 v[12:13], v34 offset:4704
	ds_read_b64_tr_b16 v[14:15], v34 offset:5280
	s_waitcnt lgkmcnt(0)
	v_add_u32_e32 v157, s72, v79
	v_lshlrev_b32_e32 v166, 16, v158
	v_and_b32_e32 v167, 0xffff0000, v158
	v_lshlrev_b32_e32 v168, 16, v159
	v_and_b32_e32 v169, 0xffff0000, v159
	v_lshlrev_b32_e32 v170, 16, v160
	v_and_b32_e32 v171, 0xffff0000, v160
	v_lshlrev_b32_e32 v172, 16, v161
	v_and_b32_e32 v173, 0xffff0000, v161
	v_lshlrev_b32_e32 v174, 16, v162
	v_and_b32_e32 v175, 0xffff0000, v162
	v_lshlrev_b32_e32 v176, 16, v163
	v_and_b32_e32 v177, 0xffff0000, v163
	v_lshlrev_b32_e32 v178, 16, v164
	v_and_b32_e32 v179, 0xffff0000, v164
	v_lshlrev_b32_e32 v180, 16, v165
	v_and_b32_e32 v181, 0xffff0000, v165
	v_mfma_f32_16x16x32_bf16 v[112:115], v[112:115], v[16:19], v[166:169]
	v_mfma_f32_16x16x32_bf16 v[44:47], v[44:47], v[16:19], v[170:173]
	v_mfma_f32_16x16x32_bf16 v[36:39], v[36:39], v[16:19], v[174:177]
	v_mfma_f32_16x16x32_bf16 v[20:23], v[20:23], v[16:19], v[178:181]
	v_mfma_f32_16x16x32_bf16 v[80:83], v[80:83], v[8:11], v[112:115]
	v_mfma_f32_16x16x32_bf16 v[40:43], v[40:43], v[8:11], v[44:47]
	v_mfma_f32_16x16x32_bf16 v[30:33], v[30:33], v[8:11], v[36:39]
	v_mfma_f32_16x16x32_bf16 v[12:15], v[12:15], v[8:11], v[20:23]
	s_nop 7
	v_cvt_pk_bf16_f32 v182, v80, v81
	v_cvt_pk_bf16_f32 v183, v82, v83
	v_cvt_pk_bf16_f32 v184, v40, v41
	v_cvt_pk_bf16_f32 v185, v42, v43
	v_cvt_pk_bf16_f32 v186, v30, v31
	v_cvt_pk_bf16_f32 v187, v32, v33
	v_cvt_pk_bf16_f32 v188, v12, v13
	v_cvt_pk_bf16_f32 v189, v14, v15
	ds_write_b64 v157, v[182:183]
	ds_write_b64 v157, v[184:185] offset:32
	ds_write_b64 v157, v[186:187] offset:64
	ds_write_b64 v157, v[188:189] offset:96
	s_mov_b64 s[72:73], 0

.LBB0_637:
	s_andn2_b64 vcc, exec, s[72:73]
	s_cbranch_vccnz .LBB0_642
	s_and_b64 vcc, exec, s[44:45]
	s_mov_b64 s[44:45], -1
	s_cbranch_vccnz .LBB0_640
	s_add_i32 s44, 0, 0x16800
	s_nop 1
	v_add3_u32 v8, s75, v24, v75
	ds_read_b128 v[8:11], v8
	v_add_u32_e32 v156, s75, v79
	ds_read_b64 v[158:159], v156
	ds_read_b64 v[160:161], v156 offset:32
	ds_read_b64_tr_b16 v[16:17], v34
	ds_read_b64_tr_b16 v[18:19], v34 offset:576
	ds_read_b64_tr_b16 v[12:13], v34 offset:32
	ds_read_b64_tr_b16 v[14:15], v34 offset:608
	s_waitcnt lgkmcnt(0)
	v_add_u32_e32 v157, s44, v79
	v_lshlrev_b32_e32 v166, 16, v158
	v_and_b32_e32 v167, 0xffff0000, v158
	v_lshlrev_b32_e32 v168, 16, v159
	v_and_b32_e32 v169, 0xffff0000, v159
	v_lshlrev_b32_e32 v170, 16, v160
	v_and_b32_e32 v171, 0xffff0000, v160
	v_lshlrev_b32_e32 v172, 16, v161
	v_and_b32_e32 v173, 0xffff0000, v161
	s_nop 1
	v_mfma_f32_16x16x32_bf16 v[16:19], v[16:19], v[8:11], v[166:169]
	v_mfma_f32_16x16x32_bf16 v[12:15], v[12:15], v[8:11], v[170:173]
	s_nop 7
	v_cvt_pk_bf16_f32 v182, v16, v17
	v_cvt_pk_bf16_f32 v183, v18, v19
	v_cvt_pk_bf16_f32 v184, v12, v13
	v_cvt_pk_bf16_f32 v185, v14, v15
	ds_write_b64 v157, v[182:183]
	ds_write_b64 v157, v[184:185] offset:32
	s_mov_b64 s[72:73], 0

.LBB0_642:
	s_waitcnt lgkmcnt(0)
	s_and_b64 vcc, exec, s[46:47]
	s_waitcnt lgkmcnt(0)
	s_barrier
	s_cbranch_vccnz .LBB0_651
	s_mov_b64 s[44:45], 0
	s_and_b64 vcc, exec, s[20:21]
	s_mov_b64 s[46:47], 0
	s_cbranch_vccz .LBB0_652
	s_add_i32 s35, 0, 0x16800
	v_add3_u32 v8, s35, v24, v75
	ds_read_b128 v[16:19], v8
	ds_read_b128 v[8:11], v8 offset:64
	v_add_u32_e32 v156, s35, v79
	ds_read_b64 v[158:159], v156
	ds_read_b64 v[160:161], v156 offset:32
	ds_read_b64 v[162:163], v156 offset:64
	ds_read_b64 v[164:165], v156 offset:96
	ds_read_b64_tr_b16 v[112:113], v25
	ds_read_b64_tr_b16 v[114:115], v25 offset:576
	ds_read_b64_tr_b16 v[80:81], v25 offset:4608
	ds_read_b64_tr_b16 v[82:83], v25 offset:5184
	ds_read_b64_tr_b16 v[44:45], v25 offset:32
	ds_read_b64_tr_b16 v[46:47], v25 offset:608
	ds_read_b64_tr_b16 v[40:41], v25 offset:4640
	ds_read_b64_tr_b16 v[42:43], v25 offset:5216
	ds_read_b64_tr_b16 v[36:37], v25 offset:64
	ds_read_b64_tr_b16 v[38:39], v25 offset:640
	ds_read_b64_tr_b16 v[30:31], v25 offset:4672
	ds_read_b64_tr_b16 v[32:33], v25 offset:5248
	ds_read_b64_tr_b16 v[20:21], v25 offset:96
	ds_read_b64_tr_b16 v[22:23], v25 offset:672
	ds_read_b64_tr_b16 v[12:13], v25 offset:4704
	ds_read_b64_tr_b16 v[14:15], v25 offset:5280
	s_waitcnt lgkmcnt(0)
	v_add_u32_e32 v157, s75, v79
	v_lshlrev_b32_e32 v166, 16, v158
	v_and_b32_e32 v167, 0xffff0000, v158
	v_lshlrev_b32_e32 v168, 16, v159
	v_and_b32_e32 v169, 0xffff0000, v159
	v_lshlrev_b32_e32 v170, 16, v160
	v_and_b32_e32 v171, 0xffff0000, v160
	v_lshlrev_b32_e32 v172, 16, v161
	v_and_b32_e32 v173, 0xffff0000, v161
	v_lshlrev_b32_e32 v174, 16, v162
	v_and_b32_e32 v175, 0xffff0000, v162
	v_lshlrev_b32_e32 v176, 16, v163
	v_and_b32_e32 v177, 0xffff0000, v163
	v_lshlrev_b32_e32 v178, 16, v164
	v_and_b32_e32 v179, 0xffff0000, v164
	v_lshlrev_b32_e32 v180, 16, v165
	v_and_b32_e32 v181, 0xffff0000, v165
	v_mfma_f32_16x16x32_bf16 v[112:115], v[112:115], v[16:19], v[166:169]
	v_mfma_f32_16x16x32_bf16 v[44:47], v[44:47], v[16:19], v[170:173]
	v_mfma_f32_16x16x32_bf16 v[36:39], v[36:39], v[16:19], v[174:177]
	v_mfma_f32_16x16x32_bf16 v[20:23], v[20:23], v[16:19], v[178:181]
	v_mfma_f32_16x16x32_bf16 v[80:83], v[80:83], v[8:11], v[112:115]
	v_mfma_f32_16x16x32_bf16 v[40:43], v[40:43], v[8:11], v[44:47]
	v_mfma_f32_16x16x32_bf16 v[30:33], v[30:33], v[8:11], v[36:39]
	v_mfma_f32_16x16x32_bf16 v[8:11], v[12:15], v[8:11], v[20:23]
	s_nop 7
	v_cvt_pk_bf16_f32 v182, v80, v81
	v_cvt_pk_bf16_f32 v183, v82, v83
	v_cvt_pk_bf16_f32 v184, v40, v41
	v_cvt_pk_bf16_f32 v185, v42, v43
	v_cvt_pk_bf16_f32 v186, v30, v31
	v_cvt_pk_bf16_f32 v187, v32, v33
	ds_write_b64 v157, v[182:183]
	ds_write_b64 v157, v[184:185] offset:32
	ds_write_b64 v157, v[186:187] offset:64
	v_add_u32_e32 v26, 0x60, v79
	s_mov_b64 s[46:47], -1
	s_branch .LBB0_652

.LBB0_652:
	s_and_b64 vcc, exec, s[44:45]
	s_cbranch_vccz .LBB0_655
	s_and_b64 vcc, exec, s[20:21]
	s_cbranch_vccz .LBB0_655
	s_add_i32 s35, 0, 0x16800
	s_nop 1
	v_add3_u32 v8, s35, v24, v75
	ds_read_b128 v[8:11], v8
	v_add_u32_e32 v156, s35, v79
	ds_read_b64 v[158:159], v156
	ds_read_b64 v[160:161], v156 offset:32
	ds_read_b64_tr_b16 v[16:17], v25
	ds_read_b64_tr_b16 v[18:19], v25 offset:576
	ds_read_b64_tr_b16 v[12:13], v25 offset:32
	ds_read_b64_tr_b16 v[14:15], v25 offset:608
	s_waitcnt lgkmcnt(0)
	v_lshlrev_b32_e32 v166, 16, v158
	v_and_b32_e32 v167, 0xffff0000, v158
	v_lshlrev_b32_e32 v168, 16, v159
	v_and_b32_e32 v169, 0xffff0000, v159
	v_lshlrev_b32_e32 v170, 16, v160
	v_and_b32_e32 v171, 0xffff0000, v160
	v_lshlrev_b32_e32 v172, 16, v161
	v_and_b32_e32 v173, 0xffff0000, v161
	s_nop 1
	v_mfma_f32_16x16x32_bf16 v[16:19], v[16:19], v[8:11], v[166:169]
	v_mfma_f32_16x16x32_bf16 v[8:11], v[12:15], v[8:11], v[170:173]
	s_nop 7
	v_cvt_pk_bf16_f32 v182, v16, v17
	v_cvt_pk_bf16_f32 v183, v18, v19
	v_add_u32_e32 v157, 0, v79
	v_add_u32_e32 v157, 0x18c00, v157
	ds_write_b64 v157, v[182:183]
	v_add_u32_e32 v26, 32, v79
	s_mov_b64 s[46:47], -1
